# speedup vs baseline: 1.0163x; 1.0163x over previous
_Z7kfinal3PKDF16_PKfS2_S2_PK15HIP_vector_typeIjLj4EES2_Pf:
	s_load_dwordx2 s[20:21], s[0:1], 0x20
	s_load_dwordx4 s[12:15], s[0:1], 0x0
	s_load_dwordx4 s[16:19], s[0:1], 0x10
	v_and_b32_e32 v136, 63, v0
	v_lshlrev_b32_e32 v136, 3, v136
	v_and_b32_e32 v137, 7, v0
	v_lshlrev_b32_e32 v137, 5, v137
	s_waitcnt lgkmcnt(0)
	global_load_dwordx2 v[88:89], v136, s[14:15]
	global_load_dwordx2 v[170:171], v136, s[14:15] offset:512
	global_load_dwordx2 v[172:173], v136, s[14:15] offset:1024
	global_load_dwordx2 v[174:175], v136, s[14:15] offset:1536
	global_load_dwordx4 v[76:79], v137, s[16:17]
	global_load_dwordx4 v[80:83], v137, s[16:17] offset:16
	global_load_dwordx4 v[84:87], v137, s[18:19]
	global_load_dwordx4 v[176:179], v137, s[18:19] offset:16
	v_lshrrev_b32_e32 v48, 6, v0
	s_bfe_u32 s24, s2, 0x20003
	s_mul_i32 s3, s24, 0x28800
	v_lshlrev_b32_e32 v118, 10, v48
	v_and_b32_e32 v1, 63, v0
	s_waitcnt lgkmcnt(0)
	s_add_u32 s6, s20, s3
	v_add_u32_e32 v2, 0, v118
	s_addc_u32 s7, s21, 0
	s_mov_b32 s50, s6
	s_mov_b32 s51, s7
	v_mov_b32_e32 v47, 0
	v_lshlrev_b32_e32 v46, 4, v1
	v_accvgpr_write_b32 a72, v2
	v_add_u32_e32 v8, 0xc600, v2
	v_and_b32_e32 v2, 0x1c0, v0
	v_lshl_add_u64 v[4:5], s[6:7], 0, v[46:47]
	v_lshlrev_b32_e32 v2, 4, v2
	v_mov_b32_e32 v3, v47
	v_readfirstlane_b32 s3, v8
	v_lshl_add_u64 v[6:7], v[4:5], 0, v[2:3]
	s_mov_b32 m0, s3
	v_or_b32_e32 v49, 8, v48
	global_load_lds_dwordx4 v[6:7], off
	s_movk_i32 s3, 0x280
	v_cmp_gt_u32_e64 s[4:5], s3, v0
	v_lshlrev_b32_e32 v90, 10, v49
	s_and_saveexec_b64 s[8:9], s[4:5]
	s_cbranch_execz .LBB3_2
	v_add_u32_e32 v3, 0, v90
	v_add_u32_e32 v3, 0xc600, v3
	v_mov_b32_e32 v91, v47
	v_readfirstlane_b32 s3, v3
	v_lshl_add_u64 v[6:7], v[4:5], 0, v[90:91]
	s_mov_b32 m0, s3
	s_nop 0
	global_load_lds_dwordx4 v[6:7], off

.LBB3_8:
	s_or_b64 exec, exec, s[6:7]
	s_lshl_b32 s3, s2, 2
	s_and_b32 s26, s3, 28
	s_lshr_b32 s3, s2, 6
	s_lshl_b32 s2, s2, 1
	s_add_i32 s26, s26, s3
	s_and_b32 s22, s2, 64
	v_lshrrev_b32_e32 v47, 3, v0
	s_movk_i32 s2, 0x20f
	s_lshl_b32 s23, s26, 2
	v_mov_b32_e32 v4, 0xffffffbe
	v_cmp_lt_u32_e64 s[6:7], s2, v0
	v_or_b32_e32 v66, 64, v47
	v_mul_lo_u16_e32 v6, 63, v66
	v_cndmask_b32_e64 v70, 0, v4, s[6:7]
	v_mov_b32_e32 v4, s23
	s_add_i32 s25, s23, -1
	s_add_i32 s27, s22, -1
	v_lshlrev_b32_e32 v28, 3, v0
	v_addc_co_u32_e64 v71, vcc, -1, v4, s[6:7]
	v_mov_b32_e32 v8, 0x7f
	v_lshrrev_b16_e32 v65, 12, v6
	v_and_b32_e32 v30, 56, v28
	v_med3_i32 v4, v71, 0, v8
	v_add3_u32 v5, s27, v47, v70
	v_mul_i32_i24_e32 v68, 0xffffffbe, v65
	v_add_u32_e32 v67, s25, v65
	v_lshlrev_b32_e32 v26, 1, v30
	v_mov_b32_e32 v27, 0
	v_med3_i32 v5, v5, 0, v8
	v_lshlrev_b32_e32 v4, 14, v4
	v_med3_i32 v6, v67, 0, v8
	v_add3_u32 v7, s27, v66, v68
	s_waitcnt lgkmcnt(0)
	v_lshl_add_u64 v[2:3], s[12:13], 0, v[26:27]
	v_lshl_or_b32 v26, v5, 7, v4
	v_med3_i32 v7, v7, 0, v8
	v_lshlrev_b32_e32 v6, 14, v6
	v_lshl_add_u64 v[4:5], v[2:3], 0, v[26:27]
	v_lshl_or_b32 v26, v7, 7, v6
	v_or_b32_e32 v62, 0x80, v47
	v_lshl_add_u64 v[6:7], v[2:3], 0, v[26:27]
	global_load_dwordx4 v[42:45], v[4:5], off
	global_load_dwordx4 v[22:25], v[6:7], off
	v_mul_lo_u16_e32 v4, 0xf9, v62
	v_or_b32_e32 v58, 0xc0, v47
	v_lshrrev_b16_e32 v61, 14, v4
	v_mul_u32_u24_e32 v6, 0x3e1, v58
	v_mul_i32_i24_e32 v64, 0xffffffbe, v61
	v_add_u32_e32 v63, s25, v61
	v_lshrrev_b32_e32 v57, 16, v6
	v_min_u32_e32 v4, 0x7f, v63
	v_add3_u32 v5, s27, v62, v64
	v_mul_i32_i24_e32 v60, 0xffffffbe, v57
	v_add_u32_e32 v59, s25, v57
	v_med3_i32 v5, v5, 0, v8
	v_lshlrev_b32_e32 v4, 14, v4
	v_min_u32_e32 v6, 0x7f, v59
	v_add3_u32 v7, s27, v58, v60
	v_lshl_or_b32 v26, v5, 7, v4
	v_med3_i32 v7, v7, 0, v8
	v_lshlrev_b32_e32 v6, 14, v6
	v_lshl_add_u64 v[4:5], v[2:3], 0, v[26:27]
	v_lshl_or_b32 v26, v7, 7, v6
	v_or_b32_e32 v54, 0x100, v47
	v_lshl_add_u64 v[6:7], v[2:3], 0, v[26:27]
	global_load_dwordx4 v[18:21], v[4:5], off
	global_load_dwordx4 v[14:17], v[6:7], off
	v_mul_u32_u24_e32 v4, 0x3e1, v54
	v_lshrrev_b32_e32 v53, 16, v4
	v_or_b32_e32 v52, 0x140, v47
	s_movk_i32 s3, 0xffbe
	v_mul_i32_i24_e32 v56, 0xffffffbe, v53
	v_add_u32_e32 v55, s25, v53
	v_mul_u32_u24_e32 v6, 0x3e1, v52
	v_min_u32_e32 v4, 0x7f, v55
	v_add3_u32 v5, s27, v54, v56
	v_mul_i32_i24_sdwa v7, v6, s3 dst_sel:DWORD dst_unused:UNUSED_PAD src0_sel:WORD_1 src1_sel:DWORD
	v_add_u32_sdwa v6, s25, v6 dst_sel:DWORD dst_unused:UNUSED_PAD src0_sel:DWORD src1_sel:WORD_1
	v_med3_i32 v5, v5, 0, v8
	v_lshlrev_b32_e32 v4, 14, v4
	v_min_u32_e32 v6, 0x7f, v6
	v_add3_u32 v7, s27, v52, v7
	v_lshl_or_b32 v26, v5, 7, v4
	v_med3_i32 v7, v7, 0, v8
	v_lshlrev_b32_e32 v6, 14, v6
	v_lshl_add_u64 v[4:5], v[2:3], 0, v[26:27]
	v_lshl_or_b32 v26, v7, 7, v6
	v_or_b32_e32 v51, 0x180, v47
	v_lshl_add_u64 v[32:33], v[2:3], 0, v[26:27]
	global_load_dwordx4 v[10:13], v[4:5], off
	global_load_dwordx4 v[6:9], v[32:33], off
	v_min_u32_e32 v4, 0x18b, v51
	s_min_u32 s2, s23, 0x7b
	v_add_u32_e32 v4, s27, v4
	v_add_u32_e32 v4, 0xfffffeb6, v4
	s_lshl_b32 s2, s2, 14
	v_min_u32_e32 v4, 0x7f, v4
	s_add_i32 s2, s2, 0x10000
	v_lshl_or_b32 v26, v4, 7, s2
	v_lshl_add_u64 v[2:3], v[2:3], 0, v[26:27]
	global_load_dwordx4 v[2:5], v[2:3], off
	s_movk_i32 s38, 0xff94
	s_movk_i32 s39, 0xffee
	s_add_i32 s40, s22, -4
	v_mov_b32_e32 v131, 0x7f
	v_mov_b32_e32 v132, 0x7c
	v_min_u32_e32 v133, 27, v50
	v_min_u32_e32 v134, 3, v48
	v_or_b32_e32 v134, 24, v134
	v_lshl_or_b32 v128, v48, 6, v1
	v_mul_u32_u24_e32 v129, 0x25f, v128
	v_lshrrev_b32_e32 v129, 16, v129
	v_mad_i32_i24 v128, v129, s38, v128
	v_mul_u32_u24_e32 v130, 0xe39, v128
	v_lshrrev_b32_e32 v130, 16, v130
	v_mad_i32_i24 v128, v130, s39, v128
	v_add_u32_e32 v130, s25, v130
	v_med3_i32 v130, v130, 0, v131
	v_lshl_add_u32 v128, v128, 2, s40
	v_med3_i32 v128, v128, 0, v132
	v_min_u32_e32 v129, 15, v129
	v_lshlrev_b32_e32 v129, 14, v129
	v_lshlrev_b32_e32 v130, 7, v130
	v_or3_b32 v94, v130, v129, v128
	v_lshl_or_b32 v128, v49, 6, v1
	v_mul_u32_u24_e32 v129, 0x25f, v128
	v_lshrrev_b32_e32 v129, 16, v129
	v_mad_i32_i24 v128, v129, s38, v128
	v_mul_u32_u24_e32 v130, 0xe39, v128
	v_lshrrev_b32_e32 v130, 16, v130
	v_mad_i32_i24 v128, v130, s39, v128
	v_add_u32_e32 v130, s25, v130
	v_med3_i32 v130, v130, 0, v131
	v_lshl_add_u32 v128, v128, 2, s40
	v_med3_i32 v128, v128, 0, v132
	v_min_u32_e32 v129, 15, v129
	v_lshlrev_b32_e32 v129, 14, v129
	v_lshlrev_b32_e32 v130, 7, v130
	v_or3_b32 v96, v130, v129, v128
	v_lshl_or_b32 v128, v133, 6, v1
	v_mul_u32_u24_e32 v129, 0x25f, v128
	v_lshrrev_b32_e32 v129, 16, v129
	v_mad_i32_i24 v128, v129, s38, v128
	v_mul_u32_u24_e32 v130, 0xe39, v128
	v_lshrrev_b32_e32 v130, 16, v130
	v_mad_i32_i24 v128, v130, s39, v128
	v_add_u32_e32 v130, s25, v130
	v_med3_i32 v130, v130, 0, v131
	v_lshl_add_u32 v128, v128, 2, s40
	v_med3_i32 v128, v128, 0, v132
	v_min_u32_e32 v129, 15, v129
	v_lshlrev_b32_e32 v129, 14, v129
	v_lshlrev_b32_e32 v130, 7, v130
	v_or3_b32 v98, v130, v129, v128
	v_lshl_or_b32 v128, v134, 6, v1
	v_mul_u32_u24_e32 v129, 0x25f, v128
	v_lshrrev_b32_e32 v129, 16, v129
	v_mad_i32_i24 v128, v129, s38, v128
	v_mul_u32_u24_e32 v130, 0xe39, v128
	v_lshrrev_b32_e32 v130, 16, v130
	v_mad_i32_i24 v128, v130, s39, v128
	v_add_u32_e32 v130, s25, v130
	v_med3_i32 v130, v130, 0, v131
	v_lshl_add_u32 v128, v128, 2, s40
	v_med3_i32 v128, v128, 0, v132
	v_min_u32_e32 v129, 15, v129
	v_lshlrev_b32_e32 v129, 14, v129
	v_lshlrev_b32_e32 v130, 7, v130
	v_or3_b32 v100, v130, v129, v128
	v_cmp_eq_u32_e32 vcc, 27, v134
	v_readfirstlane_b32 s41, v100
	s_nop 1
	v_mov_b32_e32 v135, s41
	v_cndmask_b32_e32 v100, v100, v135, vcc
	v_accvgpr_write_b32 a3, 0
	v_accvgpr_write_b32 a2, 0
	v_accvgpr_write_b32 a1, 0
	v_accvgpr_write_b32 a0, 0
	v_accvgpr_write_b32 a7, 0
	v_accvgpr_write_b32 a6, 0
	v_accvgpr_write_b32 a5, 0
	v_accvgpr_write_b32 a4, 0
	v_accvgpr_write_b32 a15, 0
	v_accvgpr_write_b32 a14, 0
	v_accvgpr_write_b32 a13, 0
	v_accvgpr_write_b32 a12, 0
	v_accvgpr_write_b32 a19, 0
	v_accvgpr_write_b32 a18, 0
	v_accvgpr_write_b32 a17, 0
	v_accvgpr_write_b32 a16, 0
	v_accvgpr_write_b32 a31, 0
	v_accvgpr_write_b32 a30, 0
	v_accvgpr_write_b32 a29, 0
	v_accvgpr_write_b32 a28, 0
	v_accvgpr_write_b32 a63, 0
	v_accvgpr_write_b32 a62, 0
	v_accvgpr_write_b32 a61, 0
	v_accvgpr_write_b32 a60, 0
	v_accvgpr_write_b32 a11, 0
	v_accvgpr_write_b32 a10, 0
	v_accvgpr_write_b32 a9, 0
	v_accvgpr_write_b32 a8, 0
	v_accvgpr_write_b32 a23, 0
	v_accvgpr_write_b32 a22, 0
	v_accvgpr_write_b32 a21, 0
	v_accvgpr_write_b32 a20, 0
	v_accvgpr_write_b32 a27, 0
	v_accvgpr_write_b32 a26, 0
	v_accvgpr_write_b32 a25, 0
	v_accvgpr_write_b32 a24, 0
	v_accvgpr_write_b32 a39, 0
	v_accvgpr_write_b32 a38, 0
	v_accvgpr_write_b32 a37, 0
	v_accvgpr_write_b32 a36, 0
	v_accvgpr_write_b32 a47, 0
	v_accvgpr_write_b32 a46, 0
	v_accvgpr_write_b32 a45, 0
	v_accvgpr_write_b32 a44, 0
	v_accvgpr_write_b32 a67, 0
	v_accvgpr_write_b32 a66, 0
	v_accvgpr_write_b32 a65, 0
	v_accvgpr_write_b32 a64, 0
	v_accvgpr_write_b32 a35, 0
	v_accvgpr_write_b32 a34, 0
	v_accvgpr_write_b32 a33, 0
	v_accvgpr_write_b32 a32, 0
	v_accvgpr_write_b32 a43, 0
	v_accvgpr_write_b32 a42, 0
	v_accvgpr_write_b32 a41, 0
	v_accvgpr_write_b32 a40, 0
	v_accvgpr_write_b32 a51, 0
	v_accvgpr_write_b32 a50, 0
	v_accvgpr_write_b32 a49, 0
	v_accvgpr_write_b32 a48, 0
	v_accvgpr_write_b32 a55, 0
	v_accvgpr_write_b32 a54, 0
	v_accvgpr_write_b32 a53, 0
	v_accvgpr_write_b32 a52, 0
	v_accvgpr_write_b32 a59, 0
	v_accvgpr_write_b32 a58, 0
	v_accvgpr_write_b32 a57, 0
	v_accvgpr_write_b32 a56, 0
	v_accvgpr_write_b32 a71, 0
	v_accvgpr_write_b32 a70, 0
	v_accvgpr_write_b32 a69, 0
	v_accvgpr_write_b32 a68, 0
	v_readfirstlane_b32 s42, v118
	v_and_b32_e32 v130, 63, v0
	v_lshlrev_b32_e32 v130, 4, v130
	v_bfe_u32 v131, v0, 6, 2
	v_bfe_u32 v132, v0, 4, 2
	v_lshrrev_b32_e32 v133, 8, v0
	v_and_b32_e32 v129, 15, v0
	v_lshl_or_b32 v133, v133, 4, v129
	s_add_i32 s43, s42, 0x2000
	s_add_i32 s44, s42, 0x4000
	v_add_u32_e32 v137, s42, v130
	v_add_u32_e32 v138, 0x2000, v137
	v_add_u32_e32 v139, 0x4000, v137
	v_add_u32_e32 v164, 0xc600, v130
	v_add_u32_e32 v165, 0x10e00, v130
	v_add_u32_e32 v166, 0x16000, v130
	v_add_u32_e32 v167, 0x1a800, v130
	v_add_u32_e32 v168, 0x1f000, v130
	s_add_u32 s52, s50, 0x9000
	s_addc_u32 s53, s51, 0
	s_add_i32 m0, s42, 0x16000
	s_nop 0
	global_load_lds_dwordx4 v137, s[52:53]
	s_add_i32 m0, s43, 0x16000
	s_nop 0
	global_load_lds_dwordx4 v138, s[52:53]
	s_cmp_lt_u32 s42, 0x800
	s_cbranch_scc0 .Lk4_sp2
	s_add_i32 m0, s44, 0x16000
	s_nop 0
	global_load_lds_dwordx4 v139, s[52:53]

.Lk4_sp4:
	v_lshl_add_u32 v128, v131, 1, 0
	v_lshl_add_u32 v128, v128, 5, v128
	v_add3_u32 v128, v128, v133, 0
	v_bitop3_b32 v129, v128, v132, 7 bitop3:0x6c
	v_lshlrev_b32_e32 v128, 7, v128
	v_lshl_or_b32 v140, v129, 4, v128
	v_xor_b32_e32 v141, 64, v140
	v_lshl_add_u32 v128, v131, 1, 1
	v_lshl_add_u32 v128, v128, 5, v128
	v_add3_u32 v128, v128, v133, 0
	v_bitop3_b32 v129, v128, v132, 7 bitop3:0x6c
	v_lshlrev_b32_e32 v128, 7, v128
	v_lshl_or_b32 v142, v129, 4, v128
	v_xor_b32_e32 v143, 64, v142
	v_lshl_add_u32 v128, v131, 1, 0
	v_lshl_add_u32 v128, v128, 5, v128
	v_add3_u32 v128, v128, v133, 1
	v_bitop3_b32 v129, v128, v132, 7 bitop3:0x6c
	v_lshlrev_b32_e32 v128, 7, v128
	v_lshl_or_b32 v144, v129, 4, v128
	v_xor_b32_e32 v145, 64, v144
	v_lshl_add_u32 v128, v131, 1, 1
	v_lshl_add_u32 v128, v128, 5, v128
	v_add3_u32 v128, v128, v133, 1
	v_bitop3_b32 v129, v128, v132, 7 bitop3:0x6c
	v_lshlrev_b32_e32 v128, 7, v128
	v_lshl_or_b32 v146, v129, 4, v128
	v_xor_b32_e32 v147, 64, v146
	v_lshl_add_u32 v128, v131, 1, 2
	v_lshl_add_u32 v128, v128, 5, v128
	v_add3_u32 v128, v128, v133, 0
	v_bitop3_b32 v129, v128, v132, 7 bitop3:0x6c
	v_lshlrev_b32_e32 v128, 7, v128
	v_lshl_or_b32 v148, v129, 4, v128
	v_xor_b32_e32 v149, 64, v148
	v_lshl_add_u32 v128, v131, 1, 3
	v_lshl_add_u32 v128, v128, 5, v128
	v_add3_u32 v128, v128, v133, 0
	v_bitop3_b32 v129, v128, v132, 7 bitop3:0x6c
	v_lshlrev_b32_e32 v128, 7, v128
	v_lshl_or_b32 v150, v129, 4, v128
	v_xor_b32_e32 v151, 64, v150
	v_lshl_add_u32 v128, v131, 1, 2
	v_lshl_add_u32 v128, v128, 5, v128
	v_add3_u32 v128, v128, v133, 1
	v_bitop3_b32 v129, v128, v132, 7 bitop3:0x6c
	v_lshlrev_b32_e32 v128, 7, v128
	v_lshl_or_b32 v152, v129, 4, v128
	v_xor_b32_e32 v153, 64, v152
	v_lshl_add_u32 v128, v131, 1, 3
	v_lshl_add_u32 v128, v128, 5, v128
	v_add3_u32 v128, v128, v133, 1
	v_bitop3_b32 v129, v128, v132, 7 bitop3:0x6c
	v_lshlrev_b32_e32 v128, 7, v128
	v_lshl_or_b32 v154, v129, 4, v128
	v_xor_b32_e32 v155, 64, v154
	v_lshl_add_u32 v128, v131, 1, 4
	v_lshl_add_u32 v128, v128, 5, v128
	v_add3_u32 v128, v128, v133, 0
	v_bitop3_b32 v129, v128, v132, 7 bitop3:0x6c
	v_lshlrev_b32_e32 v128, 7, v128
	v_lshl_or_b32 v156, v129, 4, v128
	v_xor_b32_e32 v157, 64, v156
	v_lshl_add_u32 v128, v131, 1, 5
	v_lshl_add_u32 v128, v128, 5, v128
	v_add3_u32 v128, v128, v133, 0
	v_bitop3_b32 v129, v128, v132, 7 bitop3:0x6c
	v_lshlrev_b32_e32 v128, 7, v128
	v_lshl_or_b32 v158, v129, 4, v128
	v_xor_b32_e32 v159, 64, v158
	v_lshl_add_u32 v128, v131, 1, 4
	v_lshl_add_u32 v128, v128, 5, v128
	v_add3_u32 v128, v128, v133, 1
	v_bitop3_b32 v129, v128, v132, 7 bitop3:0x6c
	v_lshlrev_b32_e32 v128, 7, v128
	v_lshl_or_b32 v160, v129, 4, v128
	v_xor_b32_e32 v161, 64, v160
	v_lshl_add_u32 v128, v131, 1, 5
	v_lshl_add_u32 v128, v128, 5, v128
	v_add3_u32 v128, v128, v133, 1
	v_bitop3_b32 v129, v128, v132, 7 bitop3:0x6c
	v_lshlrev_b32_e32 v128, 7, v128
	v_lshl_or_b32 v162, v129, 4, v128
	v_xor_b32_e32 v163, 64, v162
	s_waitcnt vmcnt(17)
	v_pk_add_f32 v[88:89], v[88:89], v[170:171]
	v_pk_add_f32 v[172:173], v[172:173], v[174:175]
	v_pk_add_f32 v[26:27], v[88:89], v[172:173]
	s_nop 1
	v_mov_b32_dpp v28, v26 row_shr:1 row_mask:0xf bank_mask:0xf bound_ctrl:1
	v_mov_b32_dpp v29, v27 row_shr:1 row_mask:0xf bank_mask:0xf bound_ctrl:1
	v_pk_add_f32 v[26:27], v[26:27], v[28:29]
	v_mov_b32_e32 v34, 0
	v_mov_b32_e32 v35, 0
	v_mov_b32_dpp v28, v26 row_shr:2 row_mask:0xf bank_mask:0xf bound_ctrl:1
	v_mov_b32_dpp v29, v27 row_shr:2 row_mask:0xf bank_mask:0xf bound_ctrl:1
	v_pk_add_f32 v[26:27], v[26:27], v[28:29]
	v_cmp_eq_u32_e32 vcc, 63, v1
	s_nop 0
	v_mov_b32_dpp v28, v26 row_shr:4 row_mask:0xf bank_mask:0xf bound_ctrl:1
	v_mov_b32_dpp v29, v27 row_shr:4 row_mask:0xf bank_mask:0xf bound_ctrl:1
	v_pk_add_f32 v[26:27], v[26:27], v[28:29]
	s_nop 1
	v_mov_b32_dpp v28, v26 row_shr:8 row_mask:0xf bank_mask:0xf bound_ctrl:1
	v_mov_b32_dpp v29, v27 row_shr:8 row_mask:0xf bank_mask:0xf bound_ctrl:1
	v_pk_add_f32 v[28:29], v[26:27], v[28:29]
	v_mov_b32_e32 v27, 0
	v_mov_b32_e32 v26, 0
	v_mov_b32_dpp v34, v28 row_bcast:15 row_mask:0xa bank_mask:0xf
	v_mov_b32_dpp v35, v29 row_bcast:15 row_mask:0xa bank_mask:0xf
	v_pk_add_f32 v[28:29], v[28:29], v[34:35]
	s_nop 1
	v_mov_b32_dpp v26, v28 row_bcast:31 row_mask:0xc bank_mask:0xf
	v_mov_b32_dpp v27, v29 row_bcast:31 row_mask:0xc bank_mask:0xf
	v_pk_add_f32 v[26:27], v[28:29], v[26:27]
	s_mov_b32 s2, 0xf800000
	s_nop 0
	v_readlane_b32 s46, v26, 63
	v_readlane_b32 s47, v27, 63
	s_nop 3
	v_mov_b32_e32 v26, s46
	v_mov_b32_e32 v27, s47
	v_mul_f32_e32 v26, 0x35800000, v26
	v_mul_f32_e32 v27, 0x35800000, v27
	v_fma_f32 v27, -v26, v26, v27
	v_add_f32_e32 v27, 0x3727c5ac, v27
	v_mul_f32_e32 v28, 0x4f800000, v27
	v_cmp_gt_f32_e32 vcc, s2, v27
	s_nop 1
	v_cndmask_b32_e32 v27, v27, v28, vcc
	v_sqrt_f32_e32 v28, v27
	s_nop 0
	v_add_u32_e32 v29, -1, v28
	v_fma_f32 v33, -v29, v28, v27
	v_cmp_ge_f32_e64 s[2:3], 0, v33
	v_add_u32_e32 v33, 1, v28
	s_nop 0
	v_cndmask_b32_e64 v29, v28, v29, s[2:3]
	v_fma_f32 v28, -v33, v28, v27
	v_cmp_lt_f32_e64 s[2:3], 0, v28
	s_nop 1
	v_cndmask_b32_e64 v28, v29, v33, s[2:3]
	v_mul_f32_e32 v29, 0x37800000, v28
	v_cndmask_b32_e32 v28, v28, v29, vcc
	v_mov_b32_e32 v29, 0x260
	v_cmp_class_f32_e32 vcc, v27, v29
	s_nop 1
	v_cndmask_b32_e32 v27, v28, v27, vcc
	v_div_scale_f32 v28, s[2:3], v27, v27, 1.0
	v_rcp_f32_e32 v29, v28
	s_nop 0
	v_fma_f32 v33, -v28, v29, 1.0
	v_fmac_f32_e32 v29, v33, v29
	v_div_scale_f32 v33, vcc, 1.0, v27, 1.0
	v_mul_f32_e32 v34, v33, v29
	v_fma_f32 v35, -v28, v34, v33
	v_fmac_f32_e32 v34, v35, v29
	v_fma_f32 v28, -v28, v34, v33
	v_div_fmas_f32 v28, v28, v29, v34
	v_div_fixup_f32 v27, v28, v27, 1.0
	v_mov_b32_e32 v169, v26
	v_mov_b32_e32 v170, v27
	v_mul_f32_e32 v26, v76, v170
	v_mul_f32_e32 v27, v77, v170
	v_mul_f32_e32 v28, v78, v170
	v_mul_f32_e32 v29, v79, v170
	v_mul_f32_e32 v34, v80, v170
	v_mul_f32_e32 v35, v81, v170
	v_mul_f32_e32 v36, v82, v170
	v_mul_f32_e32 v37, v83, v170
	v_fma_f32 v30, -v169, v26, v84
	v_fma_f32 v31, -v169, v27, v85
	v_fma_f32 v32, -v169, v28, v86
	v_fma_f32 v33, -v169, v29, v87
	v_fma_f32 v38, -v169, v34, v176
	v_fma_f32 v39, -v169, v35, v177
	v_fma_f32 v40, -v169, v36, v178
	v_fma_f32 v41, -v169, v37, v179
	s_waitcnt vmcnt(6)
	v_fma_mixlo_f16 v72, v42, v26, v30 op_sel_hi:[1,0,0]
	v_fma_mixhi_f16 v72, v42, v27, v31 op_sel:[1,0,0] op_sel_hi:[1,0,0]
	v_pk_max_f16 v72, v72, 0
	v_add3_u32 v42, v70, v47, s27
	v_add_u16_e32 v70, v70, v47
	v_bfe_u32 v69, v0, 3, 1
	v_max_u32_e32 v42, v71, v42
	v_cndmask_b32_e64 v71, 0, 2, s[6:7]
	v_ashrrev_i16_e32 v70, 1, v70
	v_or_b32_e32 v71, v71, v69
	v_bfe_i32 v70, v70, 0, 16
	v_mad_u32_u24 v70, v71, 33, v70
	v_lshlrev_b32_e32 v71, 7, v70
	v_xor_b32_e32 v70, v70, v0
	s_movk_i32 s10, 0x80
	v_lshlrev_b32_e32 v70, 4, v70
	v_cmp_gt_u32_e32 vcc, s10, v42
	v_and_b32_e32 v70, 0x70, v70
	v_fma_mixlo_f16 v73, v43, v28, v32 op_sel_hi:[1,0,0]
	v_fma_mixhi_f16 v73, v43, v29, v33 op_sel:[1,0,0] op_sel_hi:[1,0,0]
	v_pk_max_f16 v73, v73, 0
	s_waitcnt lgkmcnt(0)
	v_fma_mixlo_f16 v74, v44, v34, v38 op_sel_hi:[1,0,0]
	v_fma_mixhi_f16 v74, v44, v35, v39 op_sel:[1,0,0] op_sel_hi:[1,0,0]
	v_pk_max_f16 v74, v74, 0
	v_fma_mixlo_f16 v75, v45, v36, v40 op_sel_hi:[1,0,0]
	v_fma_mixhi_f16 v75, v45, v37, v41 op_sel:[1,0,0] op_sel_hi:[1,0,0]
	v_pk_max_f16 v75, v75, 0
	v_add3_u32 v70, 0, v71, v70
	v_cndmask_b32_e32 v42, 0, v72, vcc
	v_cndmask_b32_e32 v43, 0, v73, vcc
	v_cndmask_b32_e32 v44, 0, v74, vcc
	v_cndmask_b32_e32 v45, 0, v75, vcc
	v_add_u32_e32 v66, v68, v66
	ds_write_b128 v70, v[42:45]
	v_fma_mixlo_f16 v42, v22, v26, v30 op_sel_hi:[1,0,0]
	v_fma_mixhi_f16 v42, v22, v27, v31 op_sel:[1,0,0] op_sel_hi:[1,0,0]
	v_pk_max_f16 v42, v42, 0
	v_add_u32_e32 v22, s27, v66
	v_max_u32_e32 v22, v67, v22
	v_fma_mixlo_f16 v43, v23, v28, v32 op_sel_hi:[1,0,0]
	v_fma_mixhi_f16 v43, v23, v29, v33 op_sel:[1,0,0] op_sel_hi:[1,0,0]
	v_pk_max_f16 v43, v43, 0
	v_cmp_gt_u32_e32 vcc, s10, v22
	v_fma_mixlo_f16 v44, v24, v34, v38 op_sel_hi:[1,0,0]
	v_fma_mixhi_f16 v44, v24, v35, v39 op_sel:[1,0,0] op_sel_hi:[1,0,0]
	v_pk_max_f16 v44, v44, 0
	v_fma_mixlo_f16 v45, v25, v36, v40 op_sel_hi:[1,0,0]
	v_fma_mixhi_f16 v45, v25, v37, v41 op_sel:[1,0,0] op_sel_hi:[1,0,0]
	v_pk_max_f16 v45, v45, 0
	s_load_dwordx2 s[2:3], s[0:1], 0x28
	s_movk_i32 s6, 0x260
	v_cndmask_b32_e32 v22, 0, v42, vcc
	v_cndmask_b32_e32 v23, 0, v43, vcc
	v_lshl_or_b32 v42, v65, 1, v69
	v_ashrrev_i32_e32 v43, 1, v66
	v_mad_u32_u24 v42, v42, 33, v43
	v_lshlrev_b32_e32 v43, 7, v42
	v_xor_b32_e32 v42, v42, v0
	v_lshlrev_b32_e32 v42, 4, v42
	v_and_b32_e32 v42, 0x70, v42
	v_cndmask_b32_e32 v24, 0, v44, vcc
	v_cndmask_b32_e32 v25, 0, v45, vcc
	v_add3_u32 v42, 0, v43, v42
	ds_write_b128 v42, v[22:25]
	v_add_u32_e32 v42, v64, v62
	v_fma_mixlo_f16 v22, v18, v26, v30 op_sel_hi:[1,0,0]
	v_fma_mixhi_f16 v22, v18, v27, v31 op_sel:[1,0,0] op_sel_hi:[1,0,0]
	v_pk_max_f16 v22, v22, 0
	v_add_u32_e32 v18, s27, v42
	v_max_u32_e32 v18, v63, v18
	v_fma_mixlo_f16 v23, v19, v28, v32 op_sel_hi:[1,0,0]
	v_fma_mixhi_f16 v23, v19, v29, v33 op_sel:[1,0,0] op_sel_hi:[1,0,0]
	v_pk_max_f16 v23, v23, 0
	v_cmp_gt_u32_e32 vcc, s10, v18
	v_fma_mixlo_f16 v24, v20, v34, v38 op_sel_hi:[1,0,0]
	v_fma_mixhi_f16 v24, v20, v35, v39 op_sel:[1,0,0] op_sel_hi:[1,0,0]
	v_pk_max_f16 v24, v24, 0
	v_fma_mixlo_f16 v25, v21, v36, v40 op_sel_hi:[1,0,0]
	v_fma_mixhi_f16 v25, v21, v37, v41 op_sel:[1,0,0] op_sel_hi:[1,0,0]
	v_pk_max_f16 v25, v25, 0
	s_nop 1
	v_cndmask_b32_e32 v18, 0, v22, vcc
	v_cndmask_b32_e32 v19, 0, v23, vcc
	v_lshl_or_b32 v22, v61, 1, v69
	v_ashrrev_i32_e32 v23, 1, v42
	v_mad_u32_u24 v22, v22, 33, v23
	v_lshlrev_b32_e32 v23, 7, v22
	v_xor_b32_e32 v22, v22, v0
	v_lshlrev_b32_e32 v22, 4, v22
	v_and_b32_e32 v22, 0x70, v22
	v_cndmask_b32_e32 v20, 0, v24, vcc
	v_cndmask_b32_e32 v21, 0, v25, vcc
	v_add3_u32 v22, 0, v23, v22
	ds_write_b128 v22, v[18:21]
	v_add_u32_e32 v22, v60, v58
	v_fma_mixlo_f16 v18, v14, v26, v30 op_sel_hi:[1,0,0]
	v_fma_mixhi_f16 v18, v14, v27, v31 op_sel:[1,0,0] op_sel_hi:[1,0,0]
	v_pk_max_f16 v18, v18, 0
	v_add_u32_e32 v14, s27, v22
	v_max_u32_e32 v14, v59, v14
	v_fma_mixlo_f16 v19, v15, v28, v32 op_sel_hi:[1,0,0]
	v_fma_mixhi_f16 v19, v15, v29, v33 op_sel:[1,0,0] op_sel_hi:[1,0,0]
	v_pk_max_f16 v19, v19, 0
	v_cmp_gt_u32_e32 vcc, s10, v14
	v_fma_mixlo_f16 v20, v16, v34, v38 op_sel_hi:[1,0,0]
	v_fma_mixhi_f16 v20, v16, v35, v39 op_sel:[1,0,0] op_sel_hi:[1,0,0]
	v_pk_max_f16 v20, v20, 0
	v_fma_mixlo_f16 v21, v17, v36, v40 op_sel_hi:[1,0,0]
	v_fma_mixhi_f16 v21, v17, v37, v41 op_sel:[1,0,0] op_sel_hi:[1,0,0]
	v_pk_max_f16 v21, v21, 0
	s_nop 1
	v_cndmask_b32_e32 v14, 0, v18, vcc
	v_cndmask_b32_e32 v15, 0, v19, vcc
	v_lshl_or_b32 v18, v57, 1, v69
	v_ashrrev_i32_e32 v19, 1, v22
	v_mad_u32_u24 v18, v18, 33, v19
	v_lshlrev_b32_e32 v19, 7, v18
	v_xor_b32_e32 v18, v18, v0
	v_lshlrev_b32_e32 v18, 4, v18
	v_and_b32_e32 v18, 0x70, v18
	v_cndmask_b32_e32 v16, 0, v20, vcc
	v_cndmask_b32_e32 v17, 0, v21, vcc
	v_add3_u32 v18, 0, v19, v18
	ds_write_b128 v18, v[14:17]
	v_add_u32_e32 v18, v56, v54
	v_fma_mixlo_f16 v14, v10, v26, v30 op_sel_hi:[1,0,0]
	v_fma_mixhi_f16 v14, v10, v27, v31 op_sel:[1,0,0] op_sel_hi:[1,0,0]
	v_pk_max_f16 v14, v14, 0
	v_add_u32_e32 v10, s27, v18
	v_max_u32_e32 v10, v55, v10
	v_fma_mixlo_f16 v15, v11, v28, v32 op_sel_hi:[1,0,0]
	v_fma_mixhi_f16 v15, v11, v29, v33 op_sel:[1,0,0] op_sel_hi:[1,0,0]
	v_pk_max_f16 v15, v15, 0
	v_cmp_gt_u32_e32 vcc, s10, v10
	v_fma_mixlo_f16 v16, v12, v34, v38 op_sel_hi:[1,0,0]
	v_fma_mixhi_f16 v16, v12, v35, v39 op_sel:[1,0,0] op_sel_hi:[1,0,0]
	v_pk_max_f16 v16, v16, 0
	v_fma_mixlo_f16 v17, v13, v36, v40 op_sel_hi:[1,0,0]
	v_fma_mixhi_f16 v17, v13, v37, v41 op_sel:[1,0,0] op_sel_hi:[1,0,0]
	v_pk_max_f16 v17, v17, 0
	s_nop 1
	v_cndmask_b32_e32 v10, 0, v14, vcc
	v_cndmask_b32_e32 v11, 0, v15, vcc
	v_lshl_or_b32 v14, v53, 1, v69
	v_ashrrev_i32_e32 v15, 1, v18
	v_mad_u32_u24 v14, v14, 33, v15
	v_lshlrev_b32_e32 v15, 7, v14
	v_xor_b32_e32 v14, v14, v0
	v_lshlrev_b32_e32 v14, 4, v14
	v_and_b32_e32 v14, 0x70, v14
	v_cndmask_b32_e32 v12, 0, v16, vcc
	v_cndmask_b32_e32 v13, 0, v17, vcc
	v_add3_u32 v14, 0, v15, v14
	v_cmp_gt_u32_e32 vcc, s6, v0
	ds_write_b128 v14, v[10:13]
	v_fma_mixlo_f16 v10, v6, v26, v30 op_sel_hi:[1,0,0]
	v_fma_mixhi_f16 v10, v6, v27, v31 op_sel:[1,0,0] op_sel_hi:[1,0,0]
	v_pk_max_f16 v10, v10, 0
	v_fma_mixlo_f16 v6, v7, v28, v32 op_sel_hi:[1,0,0]
	v_fma_mixhi_f16 v6, v7, v29, v33 op_sel:[1,0,0] op_sel_hi:[1,0,0]
	v_pk_max_f16 v6, v6, 0
	v_fma_mixlo_f16 v7, v8, v34, v38 op_sel_hi:[1,0,0]
	v_fma_mixhi_f16 v7, v8, v35, v39 op_sel:[1,0,0] op_sel_hi:[1,0,0]
	v_pk_max_f16 v7, v7, 0
	v_fma_mixlo_f16 v8, v9, v36, v40 op_sel_hi:[1,0,0]
	v_fma_mixhi_f16 v8, v9, v37, v41 op_sel:[1,0,0] op_sel_hi:[1,0,0]
	v_pk_max_f16 v8, v8, 0
	s_and_saveexec_b64 s[6:7], vcc
	s_cbranch_execz .LBB3_18
	v_mul_u32_u24_e32 v9, 0x3e1, v52
	v_lshrrev_b32_e32 v9, 16, v9
	s_movk_i32 s11, 0xffbe
	v_mad_i32_i24 v14, v9, s11, v52
	v_add_u32_e32 v11, s25, v9
	v_add_u32_e32 v12, s27, v14
	v_max_u32_e32 v11, v11, v12
	v_cmp_gt_u32_e32 vcc, s10, v11
	s_nop 1
	v_cndmask_b32_e32 v11, 0, v6, vcc
	v_cndmask_b32_e32 v12, 0, v7, vcc
	v_lshl_or_b32 v6, v9, 1, v69
	v_ashrrev_i32_e32 v7, 1, v14
	v_mad_u32_u24 v6, v6, 33, v7
	v_lshlrev_b32_e32 v7, 7, v6
	v_xor_b32_e32 v6, v6, v0
	v_lshlrev_b32_e32 v6, 4, v6
	v_and_b32_e32 v6, 0x70, v6
	v_cndmask_b32_e32 v10, 0, v10, vcc
	v_cndmask_b32_e32 v13, 0, v8, vcc
	v_add3_u32 v6, 0, v7, v6
	ds_write_b128 v6, v[10:13]
